# attention queue hands conversion items out 2-of-5 (layers 1,2) / 3-of-5 (layer 0): all conversions issued before the attention items run out, no empty tickets, short-item tail
# speedup vs baseline: 1.0117x; 1.0035x over previous
.LBB0_789:
	s_or_b64 exec, exec, s[2:3]
	v_readlane_b32 s2, v253, 55
	s_waitcnt lgkmcnt(0)
	s_barrier
	v_mov_b32_e32 v0, s2
	v_readlane_b32 s2, v253, 54
	ds_read_b32 v0, v0
	s_nop 0
	v_mov_b32_e32 v1, s2
	ds_read_b32 v1, v1
	s_waitcnt lgkmcnt(0)
	s_barrier
	v_add_u32_e32 v201, 0x580, v0
	s_nop 0
	v_readfirstlane_b32 s100, v201
	v_readlane_b32 s101, v254, 38
	s_nop 3
	s_movk_i32 vcc_lo, 0x4c0
	s_movk_i32 vcc_hi, 0xbe0
	s_cmp_eq_u32 s101, 0
	s_cselect_b32 vcc_lo, 0xac0, vcc_lo
	s_cselect_b32 vcc_hi, 0x11ea, vcc_hi
	s_cmp_eq_u32 s101, 3
	s_cselect_b32 vcc_lo, 0, vcc_lo
	s_cselect_b32 vcc_hi, 0, vcc_hi
	s_add_i32 vcc_lo, s100, vcc_lo
	s_max_u32 vcc_lo, vcc_lo, vcc_hi
	v_mov_b32_e32 v201, vcc_lo
	v_readfirstlane_b32 s30, v0
	v_cmp_ge_i32_e32 vcc, v1, v201
	v_readfirstlane_b32 s24, v1
	s_cbranch_vccnz .LBB0_931
	s_add_u32 s31, s4, 0x37b00000
	s_addc_u32 s34, s5, 0
	s_add_i32 s35, s30, 0x480
	s_add_u32 s44, s4, 0x61800000
	s_addc_u32 s45, s5, 0
	s_add_u32 s46, s4, 0x42c00000
	s_addc_u32 s47, s5, 0
	s_add_u32 s10, s4, 0x66d00000
	s_addc_u32 s11, s5, 0
	s_add_u32 s48, s4, 0x61640000
	s_movk_i32 s2, 0x100
	s_addc_u32 s49, s5, 0
	v_cmp_gt_i32_e64 s[38:39], s2, v199
	s_add_i32 s2, 0, 0x14800
	v_add_u32_e32 v214, s2, v200
	s_add_i32 s2, 0, 0x16800
	s_cmp_lg_u32 0, -1
	v_lshlrev_b32_e32 v3, 1, v199
	v_lshlrev_b32_e32 v211, 4, v199
	s_cselect_b32 s3, 0, 0
	v_lshlrev_b32_e32 v0, 3, v199
	v_lshlrev_b32_e32 v1, 10, v101
	v_lshlrev_b32_e32 v2, 4, v198
	v_and_b32_e32 v3, 32, v3
	v_and_b32_e32 v5, 0xc0, v211
	s_addk_i32 s3, 0x6000
	v_and_b32_e32 v210, 24, v0
	v_lshl_or_b32 v5, v101, 8, v5
	v_add3_u32 v213, 0, v1, v2
	v_add_u32_e32 v1, s3, v3
	v_add3_u32 v217, v1, v210, v5
	v_lshrrev_b32_e32 v1, 3, v100
	v_lshl_add_u32 v215, v198, 2, s2
	v_and_b32_e32 v218, 56, v0
	v_lshl_add_u32 v220, v1, 2, s2
	s_add_i32 s2, 0, 0x14a00
	v_add_u32_e32 v4, 0, v3
	v_lshlrev_b32_e32 v96, 1, v218
	v_add_u32_e32 v221, s2, v200
	s_add_i32 s2, 0, 0x14900
	v_ashrrev_i32_e32 v203, 31, v202
	v_lshlrev_b32_e32 v208, 9, v100
	v_lshrrev_b32_e32 v209, 2, v100
	v_add3_u32 v212, v4, v210, v5
	v_cmp_gt_u32_e64 s[40:41], 32, v100
	v_cmp_lt_u32_e64 s[42:43], 31, v100
	v_or_b32_e32 v216, 0xc0, v206
	v_lshl_add_u64 v[204:205], s[4:5], 0, v[96:97]
	v_lshlrev_b32_e32 v219, 7, v1
	v_add_u32_e32 v222, s2, v200
	v_lshlrev_b32_e32 v96, 1, v98
	s_branch .LBB0_792

.LBB0_796:
	s_or_b64 exec, exec, s[2:3]
	v_readlane_b32 s101, v254, 38
	s_nop 3
	s_cmp_eq_u32 s101, 3
	s_cbranch_scc1 .Lc3_attn
	s_cmp_eq_u32 s101, 0
	s_cbranch_scc1 .Lc3_l0
	s_cmpk_lt_u32 s24, 0xbe0
	s_cbranch_scc0 .Lc3_late
	s_mul_hi_u32 s101, s24, 0xcccccccd
	s_lshr_b32 s101, s101, 2
	s_mul_i32 s2, s101, 5
	s_sub_i32 s2, s24, s2
	s_lshl_b32 s101, s101, 1
	s_cmp_eq_u32 s2, 1
	s_cbranch_scc1 .Lc3_entry
	s_cmp_eq_u32 s2, 3
	s_cbranch_scc0 .Lc3_r5a
	s_add_i32 s101, s101, 1
	s_branch .Lc3_entry
.Lc3_r5a:
	s_cmp_gt_u32 s2, 1
	s_addc_u32 s101, s101, 0
	s_cmp_gt_u32 s2, 3
	s_addc_u32 s101, s101, 0
	s_sub_i32 s24, s24, s101
	s_branch .Lc3_chk

.Lc3_l0:
	s_cmpk_lt_u32 s24, 0x11ea
	s_cbranch_scc0 .Lc3_late0
	s_mul_hi_u32 s101, s24, 0xcccccccd
	s_lshr_b32 s101, s101, 2
	s_mul_i32 s2, s101, 5
	s_sub_i32 s2, s24, s2
	s_mul_i32 s101, s101, 3
	s_bitcmp0_b32 s2, 0
	s_cbranch_scc0 .Lc3_r5b
	s_lshr_b32 s2, s2, 1
	s_add_i32 s101, s101, s2
	s_branch .Lc3_entry
.Lc3_r5b:
	s_add_i32 s2, s2, 1
	s_lshr_b32 s2, s2, 1
	s_add_i32 s101, s101, s2
	s_sub_i32 s24, s24, s101
	s_branch .Lc3_chk
